# v15 but P0 expert f32 loads without nt (default cache policy)
# baseline (speedup 1.0000x reference)
; #define MOE_LOAD(v, it) do { _Pragma("unroll") for (int i_ = 0; i_ < 64; ++i_) v[i_] = __builtin_nontemporal_load((it).src + (size_t)(2 * i_) * (it).stride); } while (0)
;     ...
;         const int nmine = (NMOE - gw + NGW - 1) / NGW;
;         const int last = gw + (nmine - 1) * NGW;
;         MoeItem ia = moe_item(wg, wu, wd, win, wout, wpn, wpd, F.ws, gw, F.lane), ib = ia;
;         MOE_LOAD(va, ia);
;         for (int j = 0; j < nmine; j += 2) {
.LBB0_77:
	s_mul_i32 s5, s47, s6
	s_sub_i32 s5, s7, s5
	s_xor_b32 s4, s68, s4
	s_add_i32 s7, s47, 1
	s_sub_i32 s43, s5, s6
	s_cmp_ge_u32 s5, s6
	s_cselect_b32 s7, s7, s47
	s_cselect_b32 s5, s43, s5
	s_add_i32 s43, s7, 1
	s_cmp_ge_u32 s5, s6
	s_cselect_b32 s5, s43, s7
	s_xor_b32 s5, s5, s4
	s_sub_i32 s6, s5, s4
	s_cmp_lt_i32 s6, 1
	s_cbranch_scc1 .LBB0_130
; #define MOE_LOAD(v, it) do { _Pragma("unroll") for (int i_ = 0; i_ < 64; ++i_) v[i_] = __builtin_nontemporal_load((it).src + (size_t)(2 * i_) * (it).stride); } while (0)
;     ...
;         const int nmine = (NMOE - gw + NGW - 1) / NGW;
;         const int last = gw + (nmine - 1) * NGW;
;         MoeItem ia = moe_item(wg, wu, wd, win, wout, wpn, wpd, F.ws, gw, F.lane), ib = ia;
;         MOE_LOAD(va, ia);
;         for (int j = 0; j < nmine; j += 2) {
	s_add_i32 s4, s6, -1
	s_mul_i32 s7, s4, s72
	s_add_i32 s7, s7, s3
	s_mul_i32 s4, s44, 0x1f8
	s_lshl_b64 s[44:45], s[44:45], 3
	s_mov_b32 s5, 0
	s_sub_u32 s44, 0, s44
	v_lshl_add_u64 v[8:9], v[4:5], 0, s[4:5]
	s_subb_u32 s45, 0, s45
	v_lshl_add_u64 v[10:11], v[8:9], 0, s[44:45]
	v_lshl_add_u64 v[12:13], v[10:11], 0, s[44:45]
	v_lshl_add_u64 v[14:15], v[12:13], 0, s[44:45]
	v_lshl_add_u64 v[16:17], v[14:15], 0, s[44:45]
	v_lshl_add_u64 v[18:19], v[16:17], 0, s[44:45]
	v_lshl_add_u64 v[20:21], v[18:19], 0, s[44:45]
	v_lshl_add_u64 v[22:23], v[20:21], 0, s[44:45]
	global_load_dword v50, v[8:9], off
	global_load_dword v49, v[10:11], off
	global_load_dword v48, v[12:13], off
	global_load_dword v47, v[14:15], off
	global_load_dword v44, v[16:17], off
	global_load_dword v43, v[18:19], off
	global_load_dword v41, v[20:21], off
	global_load_dword v37, v[22:23], off
	v_lshl_add_u64 v[8:9], v[22:23], 0, s[44:45]
	v_lshl_add_u64 v[10:11], v[8:9], 0, s[44:45]
	global_load_dword v42, v[8:9], off
	global_load_dword v40, v[10:11], off
	v_lshl_add_u64 v[8:9], v[10:11], 0, s[44:45]
	global_load_dword v39, v[8:9], off
	v_lshl_add_u64 v[8:9], v[8:9], 0, s[44:45]
	global_load_dword v38, v[8:9], off
	v_lshl_add_u64 v[8:9], v[8:9], 0, s[44:45]
	global_load_dword v52, v[8:9], off
	v_lshl_add_u64 v[8:9], v[8:9], 0, s[44:45]
	global_load_dword v51, v[8:9], off
	v_lshl_add_u64 v[8:9], v[8:9], 0, s[44:45]
	global_load_dword v56, v[8:9], off
	v_lshl_add_u64 v[8:9], v[8:9], 0, s[44:45]
	global_load_dword v55, v[8:9], off
	v_lshl_add_u64 v[8:9], v[8:9], 0, s[44:45]
	global_load_dword v60, v[8:9], off
	v_lshl_add_u64 v[8:9], v[8:9], 0, s[44:45]
	global_load_dword v59, v[8:9], off
	v_lshl_add_u64 v[8:9], v[8:9], 0, s[44:45]
	global_load_dword v64, v[8:9], off
	v_lshl_add_u64 v[8:9], v[8:9], 0, s[44:45]
	global_load_dword v63, v[8:9], off
	v_lshl_add_u64 v[8:9], v[8:9], 0, s[44:45]
	global_load_dword v68, v[8:9], off
	v_lshl_add_u64 v[8:9], v[8:9], 0, s[44:45]
	global_load_dword v67, v[8:9], off
	v_lshl_add_u64 v[8:9], v[8:9], 0, s[44:45]
	global_load_dword v70, v[8:9], off
	v_lshl_add_u64 v[8:9], v[8:9], 0, s[44:45]
	global_load_dword v69, v[8:9], off
	v_lshl_add_u64 v[8:9], v[8:9], 0, s[44:45]
	global_load_dword v74, v[8:9], off
	v_lshl_add_u64 v[8:9], v[8:9], 0, s[44:45]
	global_load_dword v73, v[8:9], off
	v_lshl_add_u64 v[8:9], v[8:9], 0, s[44:45]
	global_load_dword v78, v[8:9], off
	v_lshl_add_u64 v[8:9], v[8:9], 0, s[44:45]
	global_load_dword v77, v[8:9], off
	v_lshl_add_u64 v[8:9], v[8:9], 0, s[44:45]
	global_load_dword v82, v[8:9], off
	v_lshl_add_u64 v[8:9], v[8:9], 0, s[44:45]
	global_load_dword v81, v[8:9], off
	v_lshl_add_u64 v[8:9], v[8:9], 0, s[44:45]
	global_load_dword v30, v[8:9], off
	v_lshl_add_u64 v[8:9], v[8:9], 0, s[44:45]
	global_load_dword v29, v[8:9], off
	v_lshl_add_u64 v[8:9], v[8:9], 0, s[44:45]
	global_load_dword v32, v[8:9], off
	v_lshl_add_u64 v[8:9], v[8:9], 0, s[44:45]
	global_load_dword v31, v[8:9], off
	v_lshl_add_u64 v[8:9], v[8:9], 0, s[44:45]
	global_load_dword v34, v[8:9], off
	v_lshl_add_u64 v[8:9], v[8:9], 0, s[44:45]
	global_load_dword v33, v[8:9], off
	v_lshl_add_u64 v[8:9], v[8:9], 0, s[44:45]
	global_load_dword v36, v[8:9], off
	v_lshl_add_u64 v[8:9], v[8:9], 0, s[44:45]
	global_load_dword v35, v[8:9], off
	v_lshl_add_u64 v[8:9], v[8:9], 0, s[44:45]
	global_load_dword v46, v[8:9], off
	v_lshl_add_u64 v[8:9], v[8:9], 0, s[44:45]
	global_load_dword v45, v[8:9], off
	v_lshl_add_u64 v[8:9], v[8:9], 0, s[44:45]
	global_load_dword v54, v[8:9], off
	v_lshl_add_u64 v[8:9], v[8:9], 0, s[44:45]
	global_load_dword v53, v[8:9], off
	v_lshl_add_u64 v[8:9], v[8:9], 0, s[44:45]
	global_load_dword v58, v[8:9], off
	v_lshl_add_u64 v[8:9], v[8:9], 0, s[44:45]
	global_load_dword v57, v[8:9], off
	v_lshl_add_u64 v[8:9], v[8:9], 0, s[44:45]
	global_load_dword v62, v[8:9], off
	v_lshl_add_u64 v[8:9], v[8:9], 0, s[44:45]
	global_load_dword v61, v[8:9], off
	v_lshl_add_u64 v[8:9], v[8:9], 0, s[44:45]
	global_load_dword v66, v[8:9], off
	v_lshl_add_u64 v[8:9], v[8:9], 0, s[44:45]
	global_load_dword v65, v[8:9], off
	v_lshl_add_u64 v[8:9], v[8:9], 0, s[44:45]
	global_load_dword v72, v[8:9], off
	v_lshl_add_u64 v[8:9], v[8:9], 0, s[44:45]
	global_load_dword v71, v[8:9], off
	v_lshl_add_u64 v[8:9], v[8:9], 0, s[44:45]
	global_load_dword v76, v[8:9], off
	v_lshl_add_u64 v[8:9], v[8:9], 0, s[44:45]
	global_load_dword v75, v[8:9], off
	v_lshl_add_u64 v[8:9], v[8:9], 0, s[44:45]
	global_load_dword v80, v[8:9], off
	v_lshl_add_u64 v[8:9], v[8:9], 0, s[44:45]
	global_load_dword v79, v[8:9], off
	v_lshl_add_u64 v[8:9], v[8:9], 0, s[44:45]
	global_load_dword v84, v[8:9], off
	v_lshl_add_u64 v[8:9], v[8:9], 0, s[44:45]
	global_load_dword v83, v[8:9], off
	v_lshl_add_u64 v[8:9], v[8:9], 0, s[44:45]
	global_load_dword v85, v[8:9], off
	v_lshl_add_u64 v[8:9], v[8:9], 0, s[44:45]
	global_load_dword v86, v[8:9], off
	v_lshl_add_u64 v[8:9], v[8:9], 0, s[44:45]
	global_load_dword v88, v[8:9], off
	v_lshl_add_u64 v[8:9], v[8:9], 0, s[44:45]
	global_load_dword v89, v[8:9], off
	v_lshl_add_u64 v[8:9], v[8:9], 0, s[44:45]
	global_load_dword v90, v[8:9], off
	v_lshl_add_u64 v[8:9], v[8:9], 0, s[44:45]
	global_load_dword v91, v[8:9], off
	v_lshl_add_u64 v[8:9], v[8:9], 0, s[44:45]
	global_load_dword v92, v[8:9], off
	global_load_dword v87, v[4:5], off
	v_mov_b32_e32 v5, 0
	v_mov_b32_e32 v3, v5
	v_lshlrev_b64 v[8:9], s42, v[2:3]
	v_and_b32_e32 v1, 7, v0
	v_lshl_add_u64 v[10:11], v[6:7], 0, v[8:9]
	v_lshlrev_b32_e32 v6, 2, v1
	v_lshl_add_u32 v4, v1, 11, s46
	v_bitop3_b32 v7, v2, v6, 8 bitop3:0x36
	v_xor_b32_e32 v1, v6, v2
	v_lshl_add_u32 v9, v7, 2, v4
	v_bitop3_b32 v7, v2, v6, 16 bitop3:0x36
	v_bitop3_b32 v6, v2, v6, 24 bitop3:0x36
	v_lshl_add_u32 v1, v1, 2, v4
	v_lshl_add_u32 v18, v7, 2, v4
	v_lshl_add_u32 v19, v6, 2, v4
	v_lshlrev_b32_e32 v4, 4, v0
	v_lshrrev_b32_e32 v20, 5, v170
	v_and_b32_e32 v6, 0x70, v4
	v_lshl_add_u32 v4, v20, 7, s46
	v_bitop3_b32 v8, v0, 4, 31 bitop3:0x6c
	s_add_u32 s73, s82, 0x24000000
	v_lshl_add_u32 v21, v8, 2, v4
	v_bitop3_b32 v8, v0, 8, 31 bitop3:0x6c
	s_addc_u32 s74, s83, 0
	v_lshl_add_u32 v22, v8, 2, v4
	v_bitop3_b32 v8, v0, 12, 31 bitop3:0x6c
	s_add_u32 s75, s82, 0x4000000
	v_lshl_add_u32 v23, v8, 2, v4
	v_bitop3_b32 v8, v0, 16, 31 bitop3:0x6c
	s_addc_u32 s76, s83, 0
	v_lshl_add_u32 v24, v8, 2, v4
	v_bitop3_b32 v8, v0, 20, 31 bitop3:0x6c
	s_add_u32 s77, s82, 0x2d000000
	v_lshl_add_u32 v25, v8, 2, v4
	v_bitop3_b32 v8, v0, 24, 31 bitop3:0x6c
	s_addc_u32 s78, s83, 0
	v_lshl_add_u32 v26, v8, 2, v4
	v_bitop3_b32 v8, v0, 28, 31 bitop3:0x6c
	s_add_u32 s79, s82, 0x30400000
	v_lshl_add_u32 v27, v8, 2, v4
	v_and_b32_e32 v8, 31, v0
	v_mov_b32_e32 v7, v5
	s_addc_u32 s88, s83, 0
	v_lshl_add_u32 v28, v8, 2, v4
	s_lshl_b32 s89, s33, 4
	s_mov_b32 s90, 0x2c00000
	s_mov_b32 s91, 0
	s_branch .LBB0_81

; #define MOE_LOAD(v, it) do { _Pragma("unroll") for (int i_ = 0; i_ < 64; ++i_) v[i_] = __builtin_nontemporal_load((it).src + (size_t)(2 * i_) * (it).stride); } while (0)
;     ...
;         for (int j = 0; j < nmine; j += 2) {
;             const int it1 = gw + (j + 1) * NGW, it2 = gw + (j + 2) * NGW;
;             ib = moe_item(wg, wu, wd, win, wout, wpn, wpd, F.ws, it1 <= last ? it1 : last, F.lane); MOE_LOAD(vb, ib);
;             MOE_PROC(va, ia);
;             ia = moe_item(wg, wu, wd, win, wout, wpn, wpd, F.ws, it2 <= last ? it2 : last, F.lane); MOE_LOAD(va, ia);
.LBB0_80:
	s_lshl_b64 s[68:69], s[68:69], 3
	v_lshl_add_u64 v[14:15], v[16:17], 0, s[68:69]
	global_load_dword v87, v[16:17], off
	v_lshl_add_u64 v[16:17], v[14:15], 0, s[68:69]
	v_lshl_add_u64 v[30:31], v[16:17], 0, s[68:69]
	v_lshl_add_u64 v[32:33], v[30:31], 0, s[68:69]
	v_lshl_add_u64 v[34:35], v[32:33], 0, s[68:69]
	v_lshl_add_u64 v[36:37], v[34:35], 0, s[68:69]
	v_lshl_add_u64 v[38:39], v[36:37], 0, s[68:69]
	v_lshl_add_u64 v[40:41], v[38:39], 0, s[68:69]
	global_load_dword v92, v[14:15], off
	global_load_dword v91, v[16:17], off
	global_load_dword v90, v[30:31], off
	global_load_dword v89, v[32:33], off
	global_load_dword v88, v[34:35], off
	global_load_dword v86, v[36:37], off
	global_load_dword v85, v[38:39], off
	global_load_dword v83, v[40:41], off
	v_lshl_add_u64 v[14:15], v[40:41], 0, s[68:69]
	v_lshl_add_u64 v[16:17], v[14:15], 0, s[68:69]
	global_load_dword v84, v[14:15], off
	global_load_dword v79, v[16:17], off
	v_lshl_add_u64 v[14:15], v[16:17], 0, s[68:69]
	global_load_dword v80, v[14:15], off
	v_lshl_add_u64 v[14:15], v[14:15], 0, s[68:69]
	global_load_dword v75, v[14:15], off
	v_lshl_add_u64 v[14:15], v[14:15], 0, s[68:69]
	global_load_dword v76, v[14:15], off
	v_lshl_add_u64 v[14:15], v[14:15], 0, s[68:69]
	global_load_dword v71, v[14:15], off
	v_lshl_add_u64 v[14:15], v[14:15], 0, s[68:69]
	global_load_dword v72, v[14:15], off
	v_lshl_add_u64 v[14:15], v[14:15], 0, s[68:69]
	global_load_dword v65, v[14:15], off
	v_lshl_add_u64 v[14:15], v[14:15], 0, s[68:69]
	global_load_dword v66, v[14:15], off
	v_lshl_add_u64 v[14:15], v[14:15], 0, s[68:69]
	global_load_dword v61, v[14:15], off
	v_lshl_add_u64 v[14:15], v[14:15], 0, s[68:69]
	global_load_dword v62, v[14:15], off
	v_lshl_add_u64 v[14:15], v[14:15], 0, s[68:69]
	global_load_dword v57, v[14:15], off
	v_lshl_add_u64 v[14:15], v[14:15], 0, s[68:69]
	global_load_dword v58, v[14:15], off
	v_lshl_add_u64 v[14:15], v[14:15], 0, s[68:69]
	global_load_dword v53, v[14:15], off
	v_lshl_add_u64 v[14:15], v[14:15], 0, s[68:69]
	global_load_dword v54, v[14:15], off
	v_lshl_add_u64 v[14:15], v[14:15], 0, s[68:69]
	global_load_dword v45, v[14:15], off
	v_lshl_add_u64 v[14:15], v[14:15], 0, s[68:69]
	global_load_dword v46, v[14:15], off
	v_lshl_add_u64 v[14:15], v[14:15], 0, s[68:69]
	global_load_dword v35, v[14:15], off
	v_lshl_add_u64 v[14:15], v[14:15], 0, s[68:69]
	global_load_dword v36, v[14:15], off
	v_lshl_add_u64 v[14:15], v[14:15], 0, s[68:69]
	global_load_dword v33, v[14:15], off
	v_lshl_add_u64 v[14:15], v[14:15], 0, s[68:69]
	global_load_dword v34, v[14:15], off
	v_lshl_add_u64 v[14:15], v[14:15], 0, s[68:69]
	global_load_dword v31, v[14:15], off
	v_lshl_add_u64 v[14:15], v[14:15], 0, s[68:69]
	global_load_dword v32, v[14:15], off
	v_lshl_add_u64 v[14:15], v[14:15], 0, s[68:69]
	global_load_dword v29, v[14:15], off
	v_lshl_add_u64 v[14:15], v[14:15], 0, s[68:69]
	global_load_dword v30, v[14:15], off
	v_lshl_add_u64 v[14:15], v[14:15], 0, s[68:69]
	global_load_dword v81, v[14:15], off
	v_lshl_add_u64 v[14:15], v[14:15], 0, s[68:69]
	global_load_dword v82, v[14:15], off
	v_lshl_add_u64 v[14:15], v[14:15], 0, s[68:69]
	global_load_dword v77, v[14:15], off
	v_lshl_add_u64 v[14:15], v[14:15], 0, s[68:69]
	global_load_dword v78, v[14:15], off
	v_lshl_add_u64 v[14:15], v[14:15], 0, s[68:69]
	global_load_dword v73, v[14:15], off
	v_lshl_add_u64 v[14:15], v[14:15], 0, s[68:69]
	global_load_dword v74, v[14:15], off
	v_lshl_add_u64 v[14:15], v[14:15], 0, s[68:69]
	global_load_dword v69, v[14:15], off
	v_lshl_add_u64 v[14:15], v[14:15], 0, s[68:69]
	global_load_dword v70, v[14:15], off
	v_lshl_add_u64 v[14:15], v[14:15], 0, s[68:69]
	global_load_dword v67, v[14:15], off
	v_lshl_add_u64 v[14:15], v[14:15], 0, s[68:69]
	global_load_dword v68, v[14:15], off
	v_lshl_add_u64 v[14:15], v[14:15], 0, s[68:69]
	global_load_dword v63, v[14:15], off
	v_lshl_add_u64 v[14:15], v[14:15], 0, s[68:69]
	global_load_dword v64, v[14:15], off
	v_lshl_add_u64 v[14:15], v[14:15], 0, s[68:69]
	global_load_dword v59, v[14:15], off
	v_lshl_add_u64 v[14:15], v[14:15], 0, s[68:69]
	global_load_dword v60, v[14:15], off
	v_lshl_add_u64 v[14:15], v[14:15], 0, s[68:69]
	global_load_dword v55, v[14:15], off
	v_lshl_add_u64 v[14:15], v[14:15], 0, s[68:69]
	global_load_dword v56, v[14:15], off
	v_lshl_add_u64 v[14:15], v[14:15], 0, s[68:69]
	global_load_dword v51, v[14:15], off
	v_lshl_add_u64 v[14:15], v[14:15], 0, s[68:69]
	global_load_dword v52, v[14:15], off
	v_lshl_add_u64 v[14:15], v[14:15], 0, s[68:69]
	global_load_dword v38, v[14:15], off
	v_lshl_add_u64 v[14:15], v[14:15], 0, s[68:69]
	global_load_dword v39, v[14:15], off
	v_lshl_add_u64 v[14:15], v[14:15], 0, s[68:69]
	global_load_dword v40, v[14:15], off
	v_lshl_add_u64 v[14:15], v[14:15], 0, s[68:69]
	global_load_dword v42, v[14:15], off
	v_lshl_add_u64 v[14:15], v[14:15], 0, s[68:69]
	global_load_dword v37, v[14:15], off
	v_lshl_add_u64 v[14:15], v[14:15], 0, s[68:69]
	global_load_dword v41, v[14:15], off
	v_lshl_add_u64 v[14:15], v[14:15], 0, s[68:69]
	global_load_dword v43, v[14:15], off
	v_lshl_add_u64 v[14:15], v[14:15], 0, s[68:69]
	global_load_dword v44, v[14:15], off
	v_lshl_add_u64 v[14:15], v[14:15], 0, s[68:69]
	global_load_dword v47, v[14:15], off
	v_lshl_add_u64 v[14:15], v[14:15], 0, s[68:69]
	global_load_dword v48, v[14:15], off
	v_lshl_add_u64 v[14:15], v[14:15], 0, s[68:69]
	global_load_dword v49, v[14:15], off
	v_lshl_add_u64 v[14:15], v[14:15], 0, s[68:69]
	s_waitcnt vmcnt(62)
	ds_write2st64_b32 v28, v93, v101 offset1:1
	ds_write2st64_b32 v28, v99, v100 offset0:2 offset1:3
	ds_write2st64_b32 v28, v97, v98 offset0:4 offset1:5
	ds_write2st64_b32 v28, v95, v96 offset0:6 offset1:7
	ds_write2st64_b32 v21, v94, v124 offset0:8 offset1:9
	ds_write2st64_b32 v21, v104, v114 offset0:10 offset1:11
	ds_write2st64_b32 v21, v105, v115 offset0:12 offset1:13
	ds_write2st64_b32 v21, v106, v116 offset0:14 offset1:15
	ds_write2st64_b32 v22, v107, v117 offset0:16 offset1:17
	ds_write2st64_b32 v22, v108, v118 offset0:18 offset1:19
	ds_write2st64_b32 v22, v109, v119 offset0:20 offset1:21
	ds_write2st64_b32 v22, v110, v120 offset0:22 offset1:23
	ds_write2st64_b32 v23, v111, v121 offset0:24 offset1:25
	ds_write2st64_b32 v23, v112, v122 offset0:26 offset1:27
	global_load_dword v50, v[14:15], off
	ds_write2st64_b32 v23, v102, v103 offset0:28 offset1:29
	ds_write2st64_b32 v23, v113, v123 offset0:30 offset1:31
	ds_write2st64_b32 v24, v125, v126 offset0:32 offset1:33
	ds_write2st64_b32 v24, v127, v128 offset0:34 offset1:35
	ds_write2st64_b32 v24, v129, v130 offset0:36 offset1:37
	ds_write2st64_b32 v24, v131, v132 offset0:38 offset1:39
	ds_write2st64_b32 v25, v133, v134 offset0:40 offset1:41
	ds_write2st64_b32 v25, v135, v136 offset0:42 offset1:43
	ds_write2st64_b32 v25, v137, v138 offset0:44 offset1:45
	ds_write2st64_b32 v25, v139, v140 offset0:46 offset1:47
	ds_write2st64_b32 v26, v141, v142 offset0:48 offset1:49
	ds_write2st64_b32 v26, v143, v144 offset0:50 offset1:51
	ds_write2st64_b32 v26, v146, v147 offset0:52 offset1:53
	ds_write2st64_b32 v26, v148, v149 offset0:54 offset1:55
	ds_write2st64_b32 v27, v151, v152 offset0:56 offset1:57
	ds_write2st64_b32 v27, v153, v154 offset0:58 offset1:59
	ds_write2st64_b32 v27, v155, v157 offset0:60 offset1:61
	ds_write2st64_b32 v27, v158, v159 offset0:62 offset1:63
	s_waitcnt lgkmcnt(0)
	ds_read2_b32 v[16:17], v1 offset1:32
	v_lshlrev_b64 v[14:15], s44, v[2:3]
	v_lshl_add_u64 v[12:13], v[12:13], 0, v[14:15]
	v_lshl_add_u64 v[98:99], v[12:13], 0, v[6:7]
	v_mov_b32_e32 v12, 0
	s_waitcnt lgkmcnt(0)
	v_mul_f32_e32 v4, 0x42800000, v16
	v_mul_f32_e32 v13, 0x42800000, v17
	ds_read2_b32 v[16:17], v1 offset0:64 offset1:96
	ds_read2_b32 v[94:95], v1 offset0:128 offset1:160
	v_cvt_pk_fp8_f32 v12, v4, v13
	v_lshlrev_b64 v[14:15], s46, v[2:3]
	v_lshl_add_u64 v[10:11], v[10:11], 0, v[14:15]
	s_waitcnt lgkmcnt(1)
	v_mul_f32_e32 v4, 0x42800000, v16
	v_mul_f32_e32 v13, 0x42800000, v17
	v_cvt_pk_fp8_f32 v12, v4, v13 op_sel:[0,0,1]
	s_waitcnt lgkmcnt(0)
	v_mul_f32_e32 v4, 0x42800000, v94
	ds_read2_b32 v[14:15], v1 offset0:192 offset1:224
	v_mul_f32_e32 v16, 0x42800000, v95
	v_mov_b32_e32 v13, 0
	v_cvt_pk_fp8_f32 v13, v4, v16
	ds_read2_b32 v[16:17], v145 offset1:32
	s_waitcnt lgkmcnt(1)
	v_mul_f32_e32 v4, 0x42800000, v14
	v_mul_f32_e32 v93, 0x42800000, v15
	ds_read2_b32 v[14:15], v145 offset0:64 offset1:96
	v_cvt_pk_fp8_f32 v13, v4, v93 op_sel:[0,0,1]
	s_waitcnt lgkmcnt(1)
	v_mul_f32_e32 v4, 0x42800000, v16
	v_mul_f32_e32 v93, 0x42800000, v17
	ds_read2_b32 v[16:17], v145 offset0:128 offset1:160
	s_waitcnt lgkmcnt(1)
	v_mul_f32_e32 v96, 0x42800000, v14
	v_mov_b32_e32 v14, 0
	v_cvt_pk_fp8_f32 v14, v4, v93
	v_mul_f32_e32 v97, 0x42800000, v15
	s_waitcnt lgkmcnt(0)
	v_mul_f32_e32 v4, 0x42800000, v16
	v_mul_f32_e32 v93, 0x42800000, v17
	ds_read2_b32 v[16:17], v145 offset0:192 offset1:224
	v_mov_b32_e32 v15, 0
	v_cvt_pk_fp8_f32 v15, v4, v93
	ds_read2_b32 v[94:95], v9 offset1:32
	v_cvt_pk_fp8_f32 v14, v96, v97 op_sel:[0,0,1]
	s_waitcnt lgkmcnt(1)
	v_mul_f32_e32 v4, 0x42800000, v16
	v_mul_f32_e32 v16, 0x42800000, v17
	v_cvt_pk_fp8_f32 v15, v4, v16 op_sel:[0,0,1]
	ds_read2_b32 v[16:17], v9 offset0:64 offset1:96
	s_waitcnt lgkmcnt(1)
	v_mul_f32_e32 v4, 0x42800000, v94
	v_mul_f32_e32 v93, 0x42800000, v95
	v_mov_b32_e32 v94, 0
	ds_read2_b32 v[96:97], v9 offset0:128 offset1:160
	v_cvt_pk_fp8_f32 v94, v4, v93
	global_store_dwordx4 v[98:99], v[12:15], off sc0 sc1 nt
	s_waitcnt lgkmcnt(1)
	v_mul_f32_e32 v4, 0x42800000, v16
	v_mov_b32_e32 v95, 0
	v_mul_f32_e32 v12, 0x42800000, v17
	v_cvt_pk_fp8_f32 v94, v4, v12 op_sel:[0,0,1]
	s_waitcnt lgkmcnt(0)
	v_mul_f32_e32 v4, 0x42800000, v96
	ds_read2_b32 v[12:13], v9 offset0:192 offset1:224
	v_mul_f32_e32 v14, 0x42800000, v97
	v_cvt_pk_fp8_f32 v95, v4, v14
	ds_read2_b32 v[14:15], v150 offset1:32
	v_mov_b32_e32 v96, 0
	s_waitcnt lgkmcnt(1)
;     ...
;         for (int j = 0; j < nmine; j += 2) {
	v_mul_f32_e32 v4, 0x42800000, v12
	v_mul_f32_e32 v16, 0x42800000, v13
	ds_read2_b32 v[12:13], v150 offset0:64 offset1:96
	v_cvt_pk_fp8_f32 v95, v4, v16 op_sel:[0,0,1]
	s_waitcnt lgkmcnt(1)
	v_mul_f32_e32 v4, 0x42800000, v14
	v_mul_f32_e32 v16, 0x42800000, v15
	ds_read2_b32 v[14:15], v150 offset0:128 offset1:160
	s_waitcnt lgkmcnt(1)
	v_mul_f32_e32 v17, 0x42800000, v12
	v_mul_f32_e32 v93, 0x42800000, v13
	ds_read2_b32 v[12:13], v150 offset0:192 offset1:224
	v_cvt_pk_fp8_f32 v96, v4, v16
	s_waitcnt lgkmcnt(1)
	v_mul_f32_e32 v4, 0x42800000, v14
	v_mul_f32_e32 v14, 0x42800000, v15
	v_mov_b32_e32 v97, 0
	v_cvt_pk_fp8_f32 v97, v4, v14
	s_waitcnt lgkmcnt(0)
	v_mul_f32_e32 v4, 0x42800000, v12
	v_mul_f32_e32 v12, 0x42800000, v13
	v_cvt_pk_fp8_f32 v96, v17, v93 op_sel:[0,0,1]
	v_cvt_pk_fp8_f32 v97, v4, v12 op_sel:[0,0,1]
	s_lshl_b32 s4, s42, 3
	ds_read2_b32 v[12:13], v18 offset1:32
	v_lshl_add_u64 v[16:17], v[98:99], 0, s[4:5]
	ds_read2_b32 v[14:15], v18 offset0:64 offset1:96
	global_store_dwordx4 v[16:17], v[94:97], off sc0 sc1 nt
	ds_read2_b32 v[94:95], v18 offset0:128 offset1:160
	s_waitcnt lgkmcnt(2)
	v_mul_f32_e32 v4, 0x42800000, v12
	v_mul_f32_e32 v13, 0x42800000, v13
	v_mov_b32_e32 v12, 0
	s_waitcnt lgkmcnt(1)
	v_mul_f32_e32 v93, 0x42800000, v14
	v_mul_f32_e32 v96, 0x42800000, v15
	v_cvt_pk_fp8_f32 v12, v4, v13
	s_waitcnt lgkmcnt(0)
	v_mul_f32_e32 v4, 0x42800000, v94
	v_mul_f32_e32 v94, 0x42800000, v95
	ds_read2_b32 v[14:15], v18 offset0:192 offset1:224
	v_mov_b32_e32 v13, 0
	v_cvt_pk_fp8_f32 v13, v4, v94
	ds_read2_b32 v[94:95], v156 offset1:32
	v_cvt_pk_fp8_f32 v12, v93, v96 op_sel:[0,0,1]
	s_waitcnt lgkmcnt(1)
	v_mul_f32_e32 v4, 0x42800000, v14
	v_mul_f32_e32 v14, 0x42800000, v15
	ds_read2_b32 v[96:97], v156 offset0:64 offset1:96
	v_cvt_pk_fp8_f32 v13, v4, v14 op_sel:[0,0,1]
	s_waitcnt lgkmcnt(1)
	v_mul_f32_e32 v4, 0x42800000, v94
	v_mul_f32_e32 v15, 0x42800000, v95
	v_mov_b32_e32 v14, 0
	ds_read2_b32 v[94:95], v156 offset0:128 offset1:160
	v_cvt_pk_fp8_f32 v14, v4, v15
	s_waitcnt lgkmcnt(1)
	v_mul_f32_e32 v4, 0x42800000, v96
	v_mul_f32_e32 v15, 0x42800000, v97
	ds_read2_b32 v[96:97], v156 offset0:192 offset1:224
	v_cvt_pk_fp8_f32 v14, v4, v15 op_sel:[0,0,1]
	s_waitcnt lgkmcnt(1)
	v_mul_f32_e32 v4, 0x42800000, v94
	v_mul_f32_e32 v93, 0x42800000, v95
	ds_read2_b32 v[94:95], v19 offset1:32
	s_waitcnt lgkmcnt(1)
	v_mul_f32_e32 v100, 0x42800000, v96
	v_mul_f32_e32 v101, 0x42800000, v97
	v_mov_b32_e32 v15, 0
	ds_read2_b32 v[96:97], v19 offset0:64 offset1:96
	v_cvt_pk_fp8_f32 v15, v4, v93
	s_waitcnt lgkmcnt(1)
	v_mul_f32_e32 v4, 0x42800000, v94
	v_mul_f32_e32 v93, 0x42800000, v95
	v_mov_b32_e32 v94, 0
	ds_read2_b32 v[98:99], v19 offset0:128 offset1:160
	v_cvt_pk_fp8_f32 v94, v4, v93
	s_waitcnt lgkmcnt(1)
	v_mul_f32_e32 v4, 0x42800000, v96
	v_mul_f32_e32 v93, 0x42800000, v97
	ds_read2_b32 v[96:97], v19 offset0:192 offset1:224
	v_cvt_pk_fp8_f32 v94, v4, v93 op_sel:[0,0,1]
	s_waitcnt lgkmcnt(1)
	v_mul_f32_e32 v4, 0x42800000, v98
	v_mul_f32_e32 v93, 0x42800000, v99
	v_mov_b32_e32 v95, 0
	ds_read2_b32 v[98:99], v160 offset1:32
	v_cvt_pk_fp8_f32 v95, v4, v93
	s_waitcnt lgkmcnt(1)
	v_mul_f32_e32 v4, 0x42800000, v96
	v_mul_f32_e32 v93, 0x42800000, v97
	ds_read2_b32 v[96:97], v160 offset0:64 offset1:96
	v_cvt_pk_fp8_f32 v95, v4, v93 op_sel:[0,0,1]
	s_waitcnt lgkmcnt(1)
	v_mul_f32_e32 v4, 0x42800000, v98
	v_mul_f32_e32 v93, 0x42800000, v99
	ds_read2_b32 v[98:99], v160 offset0:128 offset1:160
	v_cvt_pk_fp8_f32 v15, v100, v101 op_sel:[0,0,1]
	s_waitcnt lgkmcnt(1)
	v_mul_f32_e32 v102, 0x42800000, v96
	v_mov_b32_e32 v96, 0
	ds_read2_b32 v[100:101], v160 offset0:192 offset1:224
	v_mul_f32_e32 v103, 0x42800000, v97
	v_cvt_pk_fp8_f32 v96, v4, v93
	s_waitcnt lgkmcnt(1)
	v_mul_f32_e32 v4, 0x42800000, v98
	v_mul_f32_e32 v93, 0x42800000, v99
	v_mov_b32_e32 v97, 0
	v_cvt_pk_fp8_f32 v97, v4, v93
	s_waitcnt lgkmcnt(0)
	v_mul_f32_e32 v4, 0x42800000, v100
	v_mul_f32_e32 v93, 0x42800000, v101
	v_cvt_pk_fp8_f32 v96, v102, v103 op_sel:[0,0,1]
	v_cvt_pk_fp8_f32 v97, v4, v93 op_sel:[0,0,1]
	v_lshl_add_u64 v[16:17], v[16:17], 0, s[4:5]
	global_store_dwordx4 v[16:17], v[12:15], off sc0 sc1 nt
	s_add_i32 s91, s91, 2
	s_cmp_ge_i32 s91, s6
	v_lshl_add_u64 v[12:13], v[16:17], 0, s[4:5]
	global_store_dwordx4 v[12:13], v[94:97], off sc0 sc1 nt
	s_waitcnt lgkmcnt(0)
	s_cbranch_scc1 .LBB0_130

; #define MOE_LOAD(v, it) do { _Pragma("unroll") for (int i_ = 0; i_ < 64; ++i_) v[i_] = __builtin_nontemporal_load((it).src + (size_t)(2 * i_) * (it).stride); } while (0)
;     ...
;             ia = moe_item(wg, wu, wd, win, wout, wpn, wpd, F.ws, it2 <= last ? it2 : last, F.lane); MOE_LOAD(va, ia);
;             MOE_PROC(vb, ib);
.LBB0_105:
	s_lshl_b64 s[46:47], s[46:47], 3
	global_load_dword v93, v[16:17], off
	v_lshl_add_u64 v[16:17], v[16:17], 0, s[46:47]
	v_lshl_add_u64 v[94:95], v[16:17], 0, s[46:47]
	v_lshl_add_u64 v[96:97], v[94:95], 0, s[46:47]
	v_lshl_add_u64 v[102:103], v[96:97], 0, s[46:47]
	v_lshl_add_u64 v[104:105], v[102:103], 0, s[46:47]
	v_lshl_add_u64 v[106:107], v[104:105], 0, s[46:47]
	v_lshl_add_u64 v[108:109], v[106:107], 0, s[46:47]
	v_lshl_add_u64 v[110:111], v[108:109], 0, s[46:47]
	global_load_dword v101, v[16:17], off
	global_load_dword v99, v[94:95], off
	global_load_dword v100, v[96:97], off
	s_nop 0
	global_load_dword v97, v[102:103], off
	global_load_dword v98, v[104:105], off
	global_load_dword v95, v[106:107], off
	global_load_dword v96, v[108:109], off
	global_load_dword v94, v[110:111], off
	v_lshl_add_u64 v[16:17], v[110:111], 0, s[46:47]
	s_waitcnt vmcnt(9)
	ds_write2st64_b32 v28, v87, v92 offset1:1
	v_lshl_add_u64 v[102:103], v[16:17], 0, s[46:47]
	global_load_dword v124, v[16:17], off
	global_load_dword v104, v[102:103], off
	v_lshl_add_u64 v[16:17], v[102:103], 0, s[46:47]
	global_load_dword v114, v[16:17], off
	v_lshl_add_u64 v[16:17], v[16:17], 0, s[46:47]
	global_load_dword v105, v[16:17], off
	v_lshl_add_u64 v[16:17], v[16:17], 0, s[46:47]
	global_load_dword v115, v[16:17], off
	v_lshl_add_u64 v[16:17], v[16:17], 0, s[46:47]
	global_load_dword v106, v[16:17], off
	v_lshl_add_u64 v[16:17], v[16:17], 0, s[46:47]
	global_load_dword v116, v[16:17], off
	v_lshl_add_u64 v[16:17], v[16:17], 0, s[46:47]
	global_load_dword v107, v[16:17], off
	v_lshl_add_u64 v[16:17], v[16:17], 0, s[46:47]
	global_load_dword v117, v[16:17], off
	v_lshl_add_u64 v[16:17], v[16:17], 0, s[46:47]
	global_load_dword v108, v[16:17], off
	v_lshl_add_u64 v[16:17], v[16:17], 0, s[46:47]
	global_load_dword v118, v[16:17], off
	v_lshl_add_u64 v[16:17], v[16:17], 0, s[46:47]
	global_load_dword v109, v[16:17], off
	v_lshl_add_u64 v[16:17], v[16:17], 0, s[46:47]
	global_load_dword v119, v[16:17], off
	v_lshl_add_u64 v[16:17], v[16:17], 0, s[46:47]
	global_load_dword v110, v[16:17], off
	v_lshl_add_u64 v[16:17], v[16:17], 0, s[46:47]
	global_load_dword v120, v[16:17], off
	v_lshl_add_u64 v[16:17], v[16:17], 0, s[46:47]
	global_load_dword v111, v[16:17], off
	v_lshl_add_u64 v[16:17], v[16:17], 0, s[46:47]
	global_load_dword v121, v[16:17], off
	v_lshl_add_u64 v[16:17], v[16:17], 0, s[46:47]
	global_load_dword v112, v[16:17], off
	v_lshl_add_u64 v[16:17], v[16:17], 0, s[46:47]
	global_load_dword v122, v[16:17], off
	v_lshl_add_u64 v[16:17], v[16:17], 0, s[46:47]
	global_load_dword v102, v[16:17], off
	v_lshl_add_u64 v[16:17], v[16:17], 0, s[46:47]
	global_load_dword v103, v[16:17], off
	v_lshl_add_u64 v[16:17], v[16:17], 0, s[46:47]
	global_load_dword v113, v[16:17], off
	v_lshl_add_u64 v[16:17], v[16:17], 0, s[46:47]
	global_load_dword v123, v[16:17], off
	v_lshl_add_u64 v[16:17], v[16:17], 0, s[46:47]
	global_load_dword v125, v[16:17], off
	v_lshl_add_u64 v[16:17], v[16:17], 0, s[46:47]
	global_load_dword v126, v[16:17], off
	v_lshl_add_u64 v[16:17], v[16:17], 0, s[46:47]
	global_load_dword v127, v[16:17], off
	v_lshl_add_u64 v[16:17], v[16:17], 0, s[46:47]
	global_load_dword v128, v[16:17], off
	v_lshl_add_u64 v[16:17], v[16:17], 0, s[46:47]
	global_load_dword v129, v[16:17], off
	v_lshl_add_u64 v[16:17], v[16:17], 0, s[46:47]
	global_load_dword v130, v[16:17], off
	v_lshl_add_u64 v[16:17], v[16:17], 0, s[46:47]
	global_load_dword v131, v[16:17], off
	v_lshl_add_u64 v[16:17], v[16:17], 0, s[46:47]
	global_load_dword v132, v[16:17], off
	v_lshl_add_u64 v[16:17], v[16:17], 0, s[46:47]
	global_load_dword v133, v[16:17], off
	v_lshl_add_u64 v[16:17], v[16:17], 0, s[46:47]
	global_load_dword v134, v[16:17], off
	v_lshl_add_u64 v[16:17], v[16:17], 0, s[46:47]
	global_load_dword v135, v[16:17], off
	v_lshl_add_u64 v[16:17], v[16:17], 0, s[46:47]
	global_load_dword v136, v[16:17], off
	v_lshl_add_u64 v[16:17], v[16:17], 0, s[46:47]
	global_load_dword v137, v[16:17], off
	v_lshl_add_u64 v[16:17], v[16:17], 0, s[46:47]
	global_load_dword v138, v[16:17], off
	v_lshl_add_u64 v[16:17], v[16:17], 0, s[46:47]
	global_load_dword v139, v[16:17], off
	v_lshl_add_u64 v[16:17], v[16:17], 0, s[46:47]
	global_load_dword v140, v[16:17], off
	v_lshl_add_u64 v[16:17], v[16:17], 0, s[46:47]
	global_load_dword v141, v[16:17], off
	v_lshl_add_u64 v[16:17], v[16:17], 0, s[46:47]
	global_load_dword v142, v[16:17], off
	v_lshl_add_u64 v[16:17], v[16:17], 0, s[46:47]
	global_load_dword v143, v[16:17], off
	v_lshl_add_u64 v[16:17], v[16:17], 0, s[46:47]
	global_load_dword v144, v[16:17], off
	v_lshl_add_u64 v[16:17], v[16:17], 0, s[46:47]
	global_load_dword v146, v[16:17], off
	v_lshl_add_u64 v[16:17], v[16:17], 0, s[46:47]
	global_load_dword v147, v[16:17], off
	v_lshl_add_u64 v[16:17], v[16:17], 0, s[46:47]
	global_load_dword v148, v[16:17], off
	v_lshl_add_u64 v[16:17], v[16:17], 0, s[46:47]
	global_load_dword v149, v[16:17], off
	v_lshl_add_u64 v[16:17], v[16:17], 0, s[46:47]
	global_load_dword v151, v[16:17], off
	v_lshl_add_u64 v[16:17], v[16:17], 0, s[46:47]
	global_load_dword v152, v[16:17], off
	v_lshl_add_u64 v[16:17], v[16:17], 0, s[46:47]
	global_load_dword v153, v[16:17], off
	v_lshl_add_u64 v[16:17], v[16:17], 0, s[46:47]
	global_load_dword v154, v[16:17], off
	v_lshl_add_u64 v[16:17], v[16:17], 0, s[46:47]
	global_load_dword v155, v[16:17], off
	v_lshl_add_u64 v[16:17], v[16:17], 0, s[46:47]
	global_load_dword v157, v[16:17], off
	v_lshl_add_u64 v[16:17], v[16:17], 0, s[46:47]
	global_load_dword v158, v[16:17], off
	v_lshl_add_u64 v[16:17], v[16:17], 0, s[46:47]
	ds_write2st64_b32 v28, v91, v90 offset0:2 offset1:3
	ds_write2st64_b32 v28, v89, v88 offset0:4 offset1:5
	ds_write2st64_b32 v28, v86, v85 offset0:6 offset1:7
	ds_write2st64_b32 v21, v83, v84 offset0:8 offset1:9
	ds_write2st64_b32 v21, v79, v80 offset0:10 offset1:11
	ds_write2st64_b32 v21, v75, v76 offset0:12 offset1:13
	ds_write2st64_b32 v21, v71, v72 offset0:14 offset1:15
	ds_write2st64_b32 v22, v65, v66 offset0:16 offset1:17
	ds_write2st64_b32 v22, v61, v62 offset0:18 offset1:19
	ds_write2st64_b32 v22, v57, v58 offset0:20 offset1:21
	ds_write2st64_b32 v22, v53, v54 offset0:22 offset1:23
	ds_write2st64_b32 v23, v45, v46 offset0:24 offset1:25
	ds_write2st64_b32 v23, v35, v36 offset0:26 offset1:27
	ds_write2st64_b32 v23, v33, v34 offset0:28 offset1:29
	ds_write2st64_b32 v23, v31, v32 offset0:30 offset1:31
	ds_write2st64_b32 v24, v29, v30 offset0:32 offset1:33
	ds_write2st64_b32 v24, v81, v82 offset0:34 offset1:35
	ds_write2st64_b32 v24, v77, v78 offset0:36 offset1:37
	ds_write2st64_b32 v24, v73, v74 offset0:38 offset1:39
	ds_write2st64_b32 v25, v69, v70 offset0:40 offset1:41
	ds_write2st64_b32 v25, v67, v68 offset0:42 offset1:43
	ds_write2st64_b32 v25, v63, v64 offset0:44 offset1:45
	ds_write2st64_b32 v25, v59, v60 offset0:46 offset1:47
	ds_write2st64_b32 v26, v55, v56 offset0:48 offset1:49
	ds_write2st64_b32 v26, v51, v52 offset0:50 offset1:51
	global_load_dword v159, v[16:17], off
	ds_write2st64_b32 v26, v38, v39 offset0:52 offset1:53
	ds_write2st64_b32 v26, v40, v42 offset0:54 offset1:55
	ds_write2st64_b32 v27, v37, v41 offset0:56 offset1:57
	ds_write2st64_b32 v27, v43, v44 offset0:58 offset1:59
	ds_write2st64_b32 v27, v47, v48 offset0:60 offset1:61
	ds_write2st64_b32 v27, v49, v50 offset0:62 offset1:63
	s_waitcnt lgkmcnt(0)
	ds_read2_b32 v[16:17], v1 offset1:32
	v_mov_b32_e32 v30, 0
	ds_read2_b32 v[32:33], v1 offset0:128 offset1:160
	v_mov_b32_e32 v31, 0
	v_add_u32_e32 v145, 0x400, v1
	s_waitcnt lgkmcnt(1)
	v_mul_f32_e32 v4, 0x42800000, v16
	v_mul_f32_e32 v15, 0x42800000, v17
	ds_read2_b32 v[16:17], v1 offset0:64 offset1:96
	v_cvt_pk_fp8_f32 v30, v4, v15
	ds_read2_b32 v[34:35], v145 offset0:128 offset1:160
	v_add_u32_e32 v150, 0x400, v9
	ds_read2_b32 v[38:39], v150 offset0:128 offset1:160
	s_waitcnt lgkmcnt(2)
	v_mul_f32_e32 v4, 0x42800000, v16
	v_mul_f32_e32 v15, 0x42800000, v17
	ds_read2_b32 v[16:17], v1 offset0:192 offset1:224
	v_cvt_pk_fp8_f32 v30, v4, v15 op_sel:[0,0,1]
	v_mul_f32_e32 v4, 0x42800000, v32
	v_mul_f32_e32 v15, 0x42800000, v33
	v_cvt_pk_fp8_f32 v31, v4, v15
	s_waitcnt lgkmcnt(0)
	v_mul_f32_e32 v4, 0x42800000, v16
	v_mul_f32_e32 v15, 0x42800000, v17
	ds_read2_b32 v[16:17], v145 offset0:64 offset1:96
	ds_read2_b32 v[32:33], v145 offset1:32
	v_cvt_pk_fp8_f32 v31, v4, v15 op_sel:[0,0,1]
	v_lshl_add_u64 v[10:11], v[10:11], 0, v[6:7]
	v_add_u32_e32 v156, 0x400, v18
	s_waitcnt lgkmcnt(1)
	v_mul_f32_e32 v29, 0x42800000, v16
	v_mul_f32_e32 v36, 0x42800000, v17
	ds_read2_b32 v[16:17], v145 offset0:192 offset1:224
	s_waitcnt lgkmcnt(1)
	v_mul_f32_e32 v4, 0x42800000, v32
	v_mul_f32_e32 v15, 0x42800000, v33
	v_mov_b32_e32 v32, 0
	v_cvt_pk_fp8_f32 v32, v4, v15
	v_mul_f32_e32 v4, 0x42800000, v34
	v_mul_f32_e32 v15, 0x42800000, v35
	v_mov_b32_e32 v33, 0
	ds_read2_b32 v[34:35], v9 offset1:32
	v_cvt_pk_fp8_f32 v33, v4, v15
	s_waitcnt lgkmcnt(1)
	v_mul_f32_e32 v4, 0x42800000, v16
	v_mul_f32_e32 v15, 0x42800000, v17
	ds_read2_b32 v[16:17], v9 offset0:64 offset1:96
	v_cvt_pk_fp8_f32 v32, v29, v36 op_sel:[0,0,1]
	ds_read2_b32 v[36:37], v9 offset0:128 offset1:160
	v_cvt_pk_fp8_f32 v33, v4, v15 op_sel:[0,0,1]
	s_waitcnt lgkmcnt(2)
	v_mul_f32_e32 v4, 0x42800000, v34
	v_mul_f32_e32 v15, 0x42800000, v35
	v_mov_b32_e32 v34, 0
	v_cvt_pk_fp8_f32 v34, v4, v15
	s_waitcnt lgkmcnt(1)
	v_mul_f32_e32 v4, 0x42800000, v16
	v_mul_f32_e32 v15, 0x42800000, v17
	ds_read2_b32 v[16:17], v9 offset0:192 offset1:224
	s_waitcnt lgkmcnt(1)
	v_mul_f32_e32 v29, 0x42800000, v36
	v_mul_f32_e32 v36, 0x42800000, v37
	v_mov_b32_e32 v35, 0
	v_cvt_pk_fp8_f32 v35, v29, v36
	ds_read2_b32 v[36:37], v150 offset1:32
	v_cvt_pk_fp8_f32 v34, v4, v15 op_sel:[0,0,1]
	s_waitcnt lgkmcnt(1)
	v_mul_f32_e32 v4, 0x42800000, v16
	v_mul_f32_e32 v15, 0x42800000, v17
	ds_read2_b32 v[16:17], v150 offset0:64 offset1:96
	v_cvt_pk_fp8_f32 v35, v4, v15 op_sel:[0,0,1]
	s_waitcnt lgkmcnt(1)
	v_mul_f32_e32 v4, 0x42800000, v36
	v_mul_f32_e32 v15, 0x42800000, v37
	v_mov_b32_e32 v36, 0
	v_cvt_pk_fp8_f32 v36, v4, v15
	s_waitcnt lgkmcnt(0)
	v_mul_f32_e32 v4, 0x42800000, v16
	v_mul_f32_e32 v15, 0x42800000, v17
	ds_read2_b32 v[16:17], v150 offset0:192 offset1:224
	v_cvt_pk_fp8_f32 v36, v4, v15 op_sel:[0,0,1]
	v_mul_f32_e32 v4, 0x42800000, v38
	v_mul_f32_e32 v15, 0x42800000, v39
	v_mov_b32_e32 v37, 0
	v_cvt_pk_fp8_f32 v37, v4, v15
	s_waitcnt lgkmcnt(0)
; __device__ __forceinline__ MoeItem moe_item(const float* wg, const float* wu, const float* wd, const float* win, const float* wout, const float* wpn, const float* wpd, unsigned char* ws, int r, int lane) {
;     if (r >= NMOE_X + NGATE_IT + NWO_IT) { const int q = r - NMOE_X - NGATE_IT - NWO_IT, which = q >> 9, kb = (q >> 6) & 7, nb = q & 63; MoeItem it; it.stride = DM; it.dpitch = 1024;
;         it.src = (which ? wpd : wpn) + (size_t)(kb * 128 + (lane >> 5)) * DM + nb * 32 + (lane & 31);
;         it.dst = ws + (which ? WS_WPDFT : WS_WPNAT) + (size_t)(nb * 32) * 1024 + kb * 128 + (size_t)(lane >> 3) * 1024 + 16 * (lane & 7); return it; }
;     if (r >= NMOE_X + NGATE_IT) { const int q = r - NMOE_X - NGATE_IT, kb = q >> 6, nb = q & 63; MoeItem it; it.stride = DM; it.dpitch = DM;
;         it.src = wout + (size_t)(kb * 128 + (lane >> 5)) * DM + nb * 32 + (lane & 31);
;         it.dst = ws + WS_WO8 + (size_t)(nb * 32) * DM + kb * 128 + (size_t)(lane >> 3) * DM + 16 * (lane & 7); return it; }
;     if (r >= NMOE_X) { const int q = r - NMOE_X, kb = q / 192, nb = q % 192; MoeItem it; it.stride = INC; it.dpitch = DM;
;         const int scol = nb < 128 ? 6144 + nb * 32 : (nb < 160 ? 1024 + (nb - 128) * 32 : 3072 + (nb - 160) * 32);
;         it.src = win + (size_t)(kb * 128 + (lane >> 5)) * INC + scol + (lane & 31);
;         it.dst = ws + WS_WG8 + (size_t)(nb * 32) * DM + kb * 128 + (size_t)(lane >> 3) * DM + 16 * (lane & 7); return it; }
;     const int mat = r / MOE_IE, q = r % MOE_IE, e = mat / 3, which = mat % 3, kb = q / 64, nb = q % 64, n0 = nb * 32;
;     const float* src = (which == 0 ? wg : (which == 1 ? wu : wd)) + (size_t)e * DM * DFF + (size_t)(kb * 128 + (lane >> 5)) * DFF + n0 + (lane & 31);
;     unsigned char* dst;
;     if (which < 2) dst = ws + WS_WGUT + ((size_t)(e * 16 + (n0 >> 7)) * 256 + which * 128 + (n0 & 127)) * DM;
;     else dst = ws + WS_WDT + ((size_t)e * DM + n0) * DFF;
;     MoeItem it; it.stride = DFF; it.dpitch = DM; it.src = src; it.dst = dst + kb * 128 + (size_t)(lane >> 3) * DM + 16 * (lane & 7); return it;
	v_mul_f32_e32 v4, 0x42800000, v16
	v_mul_f32_e32 v15, 0x42800000, v17
	ds_read2_b32 v[16:17], v18 offset1:32
	v_cvt_pk_fp8_f32 v37, v4, v15 op_sel:[0,0,1]
	global_store_dwordx4 v[10:11], v[30:33], off sc0 sc1 nt
	ds_read2_b32 v[32:33], v18 offset0:64 offset1:96
	s_lshl_b64 s[38:39], s[38:39], 3
	s_waitcnt lgkmcnt(1)
	v_mul_f32_e32 v4, 0x42800000, v16
	v_mul_f32_e32 v15, 0x42800000, v17
	ds_read2_b32 v[16:17], v18 offset0:128 offset1:160
	v_mov_b32_e32 v30, 0
	v_cvt_pk_fp8_f32 v30, v4, v15
	s_waitcnt lgkmcnt(1)
	v_mul_f32_e32 v4, 0x42800000, v32
	v_mov_b32_e32 v31, 0
	s_waitcnt lgkmcnt(0)
	v_mul_f32_e32 v29, 0x42800000, v16
	v_mul_f32_e32 v32, 0x42800000, v17
	ds_read2_b32 v[16:17], v18 offset0:192 offset1:224
	v_mul_f32_e32 v15, 0x42800000, v33
	v_cvt_pk_fp8_f32 v31, v29, v32
	ds_read2_b32 v[32:33], v156 offset1:32
	v_cvt_pk_fp8_f32 v30, v4, v15 op_sel:[0,0,1]
	s_waitcnt lgkmcnt(1)
	v_mul_f32_e32 v4, 0x42800000, v16
	v_mul_f32_e32 v15, 0x42800000, v17
	ds_read2_b32 v[16:17], v156 offset0:64 offset1:96
	v_lshl_add_u64 v[10:11], v[10:11], 0, s[38:39]
	global_store_dwordx4 v[10:11], v[34:37], off sc0 sc1 nt
	ds_read2_b32 v[34:35], v156 offset0:128 offset1:160
	v_cvt_pk_fp8_f32 v31, v4, v15 op_sel:[0,0,1]
	s_waitcnt lgkmcnt(2)
	v_mul_f32_e32 v4, 0x42800000, v32
	v_mul_f32_e32 v15, 0x42800000, v33
	v_mov_b32_e32 v32, 0
	v_cvt_pk_fp8_f32 v32, v4, v15
	s_waitcnt lgkmcnt(1)
	v_mul_f32_e32 v4, 0x42800000, v16
	v_mul_f32_e32 v15, 0x42800000, v17
	ds_read2_b32 v[16:17], v156 offset0:192 offset1:224
	s_waitcnt lgkmcnt(1)
	v_mul_f32_e32 v29, 0x42800000, v34
	v_mul_f32_e32 v34, 0x42800000, v35
	v_mov_b32_e32 v33, 0
	v_cvt_pk_fp8_f32 v33, v29, v34
	ds_read2_b32 v[34:35], v19 offset1:32
	v_cvt_pk_fp8_f32 v32, v4, v15 op_sel:[0,0,1]
	s_waitcnt lgkmcnt(1)
	v_mul_f32_e32 v4, 0x42800000, v16
	v_mul_f32_e32 v15, 0x42800000, v17
	ds_read2_b32 v[16:17], v19 offset0:64 offset1:96
	ds_read2_b32 v[36:37], v19 offset0:128 offset1:160
	v_cvt_pk_fp8_f32 v33, v4, v15 op_sel:[0,0,1]
	s_waitcnt lgkmcnt(2)
	v_mul_f32_e32 v4, 0x42800000, v34
	v_mul_f32_e32 v15, 0x42800000, v35
	v_mov_b32_e32 v34, 0
	v_cvt_pk_fp8_f32 v34, v4, v15
	s_waitcnt lgkmcnt(1)
	v_mul_f32_e32 v4, 0x42800000, v16
	v_mul_f32_e32 v15, 0x42800000, v17
	ds_read2_b32 v[16:17], v19 offset0:192 offset1:224
	s_waitcnt lgkmcnt(1)
	v_mul_f32_e32 v29, 0x42800000, v36
	v_mul_f32_e32 v36, 0x42800000, v37
	v_mov_b32_e32 v35, 0
	v_add_u32_e32 v160, 0x400, v19
	v_cvt_pk_fp8_f32 v35, v29, v36
	ds_read2_b32 v[36:37], v160 offset1:32
	v_cvt_pk_fp8_f32 v34, v4, v15 op_sel:[0,0,1]
	s_waitcnt lgkmcnt(1)
	v_mul_f32_e32 v4, 0x42800000, v16
	v_mul_f32_e32 v15, 0x42800000, v17
	ds_read2_b32 v[16:17], v160 offset0:64 offset1:96
	ds_read2_b32 v[38:39], v160 offset0:128 offset1:160
	v_cvt_pk_fp8_f32 v35, v4, v15 op_sel:[0,0,1]
	s_waitcnt lgkmcnt(2)
	v_mul_f32_e32 v4, 0x42800000, v36
	v_mul_f32_e32 v15, 0x42800000, v37
	v_mov_b32_e32 v36, 0
	v_cvt_pk_fp8_f32 v36, v4, v15
	s_waitcnt lgkmcnt(1)
	v_mul_f32_e32 v4, 0x42800000, v16
	v_mul_f32_e32 v15, 0x42800000, v17
	ds_read2_b32 v[16:17], v160 offset0:192 offset1:224
	s_waitcnt lgkmcnt(1)
	v_mul_f32_e32 v29, 0x42800000, v38
	v_mul_f32_e32 v38, 0x42800000, v39
	v_mov_b32_e32 v37, 0
	v_cvt_pk_fp8_f32 v37, v29, v38
	v_cvt_pk_fp8_f32 v36, v4, v15 op_sel:[0,0,1]
	s_waitcnt lgkmcnt(0)
	v_mul_f32_e32 v4, 0x42800000, v16
	v_mul_f32_e32 v15, 0x42800000, v17
	v_cvt_pk_fp8_f32 v37, v4, v15 op_sel:[0,0,1]
	v_lshl_add_u64 v[10:11], v[10:11], 0, s[38:39]
	global_store_dwordx4 v[10:11], v[30:33], off sc0 sc1 nt
	v_lshl_add_u64 v[10:11], v[10:11], 0, s[38:39]
	global_store_dwordx4 v[10:11], v[34:37], off sc0 sc1 nt
	s_waitcnt lgkmcnt(0)
	s_add_i32 s3, s89, s3
	s_mov_b32 s96, 0
	s_min_i32 s43, s3, s7
	s_cmp_lt_i32 s43, 0x19000
	s_mov_b64 s[38:39], -1
	s_cbranch_scc0 .LBB0_126
	s_cmp_lt_i32 s43, 0x18c00
	s_cbranch_scc0 .LBB0_123
	s_cmp_lt_i32 s43, 0x18000
	s_cbranch_scc0 .LBB0_113
	s_mov_b32 s96, 1
	s_ashr_i32 s4, s43, 31
	s_lshr_b32 s4, s4, 22
	s_add_i32 s4, s43, s4
	s_ashr_i32 s39, s4, 10
	s_and_b32 s4, s4, 0xfc00
	s_sub_i32 s46, s43, s4
	s_mul_hi_i32 s4, s43, 0x2aaaaaab
	s_lshr_b32 s38, s4, 31
	s_ashr_i32 s4, s4, 9
	s_add_i32 s38, s4, s38
	s_mul_hi_i32 s4, s39, 0x55555556
	s_lshr_b32 s45, s4, 31
	s_add_i32 s4, s4, s45
	s_mul_i32 s4, s4, 3
	s_sub_i32 s4, s39, s4
	s_sext_i32_i16 s39, s46
	s_bfe_u32 s39, s39, 0x60019
	s_add_i32 s45, s46, s39
	s_and_b32 s39, s45, 0xffc0
	s_sub_i32 s39, s46, s39
	s_sext_i32_i16 s84, s39
	s_lshl_b32 s46, s84, 5
	s_ashr_i32 s39, s38, 31
	s_ashr_i32 s47, s46, 31
	s_cmp_gt_i32 s4, 1
	s_mov_b64 s[70:71], -1
	s_cbranch_scc0 .LBB0_110
	s_lshl_b64 s[68:69], s[38:39], 22
	s_lshl_b64 s[70:71], s[46:47], 11
	s_add_u32 s68, s73, s68
	s_addc_u32 s69, s74, s69
	s_add_u32 s68, s68, s70
	s_addc_u32 s69, s69, s71
	s_mov_b64 s[70:71], 0
